# P2 attention: one static s_setprio 1 for waves 4-7 (the second wave of each SIMD) for the whole phase, reset at phase end
# baseline (speedup 1.0000x reference)
.LBB0_218:
	s_cmp_lt_i32 s64, 3
	s_cselect_b64 s[0:1], -1, 0
	s_and_b64 s[22:23], s[0:1], s[4:5]
	s_andn2_b64 vcc, exec, s[22:23]
	s_mov_b32 s36, 1
	s_cbranch_vccnz .LBB0_351
	v_readlane_b32 s98, v239, 0
	s_cmp_lt_u32 s98, 0x100
	s_cbranch_scc1 .Lp2_noprio
	s_setprio 1
.Lp2_noprio:
	s_add_u32 s11, s60, 0xe000000
	s_addc_u32 s5, s61, 0
	s_add_u32 s6, s62, 0x2e000000
	s_addc_u32 s7, s63, 0
	s_add_u32 s0, s60, 0x8000000
	v_writelane_b32 v239, s0, 50
	s_addc_u32 s0, s61, 0
	v_writelane_b32 v239, s0, 52
	s_add_u32 s0, s62, 0x28000000
	v_writelane_b32 v239, s0, 54
	s_addc_u32 s0, s63, 0
	v_writelane_b32 v239, s0, 56
	s_add_u32 s0, s62, 0x30000000
	v_writelane_b32 v239, s0, 58
	s_addc_u32 s0, s63, 0
	s_add_u32 s8, s62, 0xe000000
	s_addc_u32 s9, s63, 0
	v_writelane_b32 v239, s0, 60
	s_add_u32 s0, s62, 0x36000000
	v_writelane_b32 v239, s0, 62
	s_addc_u32 s0, s63, 0
	v_writelane_b32 v238, s0, 0
	s_add_u32 s0, s62, 0x3c000000
	v_writelane_b32 v238, s0, 2
	s_addc_u32 s0, s63, 0
	v_writelane_b32 v238, s0, 4
	s_ashr_i32 s0, s96, 5
	s_ashr_i32 s1, s0, 31
	s_and_b32 s10, s96, 3
	s_lshl_b64 s[2:3], s[0:1], 21
	s_add_u32 s2, s60, s2
	s_addc_u32 s3, s61, s3
	s_lshl_b32 s4, s10, 8
	s_add_u32 s48, s2, s4
	s_addc_u32 s49, s3, 0
	s_lshl_b64 s[2:3], s[0:1], 19
	v_writelane_b32 v238, s11, 6
	s_add_u32 s1, s11, s2
	v_writelane_b32 v238, s5, 7
	s_addc_u32 s5, s5, s3
	s_lshl_b32 s34, s10, 6
	s_add_u32 s12, s1, s34
	s_addc_u32 s13, s5, 0
	s_add_u32 s1, s6, s2
	s_addc_u32 s2, s7, s3
	s_add_u32 s14, s1, s34
	s_addc_u32 s15, s2, 0
	s_mul_hi_i32 s1, s0, 0x280000
	s_mul_i32 s0, s0, 0x280000
	v_writelane_b32 v238, s6, 9
	s_add_u32 s0, s8, s0
	v_writelane_b32 v238, s7, 11
	s_addc_u32 s1, s9, s1
	v_writelane_b32 v238, s8, 13
	s_add_u32 s8, s0, s4
	v_writelane_b32 v238, s9, 15
	s_addc_u32 s9, s1, 0
	s_lshl_b32 s0, s10, 4
	s_add_u32 s44, s84, s0
	s_addc_u32 s45, s85, 0
	s_lshl_b32 s0, s96, 1
	s_and_b32 s3, s0, 56
	v_mov_b32_e32 v4, v0
	s_mov_b32 s20, 8
	s_mov_b32 s35, 0
	s_mov_b32 s55, 4
	s_movk_i32 s37, 0x400
	s_cmpk_lt_i32 s96, 0x400
	s_waitcnt vmcnt(0)
	v_readfirstlane_b32 s2, v4
	s_cbranch_scc1 .LBB0_222
	s_mov_b64 s[44:45], 0
	s_mov_b32 s5, 0
	s_cmpk_lt_u32 s96, 0x800
	s_mov_b32 s55, 1
	s_cbranch_scc1 .LBB0_223
	s_lshr_b32 s0, s96, 1
	s_and_b32 s4, s0, 14
	s_bfe_u32 s6, s96, 0x20002
	s_and_b32 s3, s0, 8
	s_cmpk_gt_u32 s96, 0xbff
	s_cselect_b64 s[0:1], -1, 0
	v_cndmask_b32_e64 v1, 0, 1, s[0:1]
	s_and_b64 s[0:1], s[0:1], exec
	s_cselect_b32 s0, 8, 4
	s_cselect_b32 s6, s4, s6
	s_movk_i32 s4, 0xf400
	s_cselect_b32 s36, 16, 4
	s_cselect_b32 s3, 0, s3
	s_cselect_b32 s20, 4, 8
	s_cselect_b32 s4, s4, 0xfffff800
	s_or_b32 s10, s10, s0
	s_mov_b32 s1, 0
	v_readfirstlane_b32 s35, v1
	s_lshl_b32 s0, s10, 6
	s_branch .LBB0_224

.LBB0_351:
	s_setprio 0
	s_cmp_gt_i32 s65, 3
	s_cselect_b64 s[0:1], -1, 0
	s_and_b64 s[2:3], s[22:23], s[0:1]
	s_andn2_b64 vcc, exec, s[2:3]
	s_cbranch_vccnz .LBB0_405
	s_waitcnt vmcnt(0)
	s_waitcnt vmcnt(0) lgkmcnt(0)
	s_barrier
	s_mov_b64 s[4:5], exec
	v_readlane_b32 s2, v239, 5
	v_readlane_b32 s3, v239, 6
	s_and_b64 s[2:3], s[4:5], s[2:3]
	s_mov_b64 exec, s[2:3]
	s_cbranch_execz .Lhw_seam2
	s_add_i32 s2, 0, 0x21160
	v_mov_b32_e32 v1, s2
	s_waitcnt vmcnt(0) expcnt(0) lgkmcnt(0)
	ds_read_b32 v3, v1
	s_add_i32 s2, 0, 0x21164
	v_mov_b32_e32 v1, s2
	ds_read_b32 v1, v1
	s_waitcnt lgkmcnt(1)
	v_cmp_ne_u32_e32 vcc, 0, v3
	s_cbranch_vccnz .LBB0_368
	v_readlane_b32 s6, v239, 1
	v_readlane_b32 s7, v239, 2
	s_load_dwordx2 s[2:3], s[6:7], 0x4
	s_add_u32 s6, s76, 0x1000
	s_addc_u32 s7, s77, 0
	s_add_u32 s8, s76, 0x1100
	s_addc_u32 s9, s77, 0
	s_add_u32 s10, s76, 0x1200
	s_addc_u32 s11, s77, 0
	s_waitcnt lgkmcnt(0)
	s_mul_i32 s2, s2, s74
	s_add_u32 s12, s76, 0x1300
	s_mul_i32 s2, s2, s3
	s_addc_u32 s13, s77, 0
	s_mov_b32 s3, 1
	v_mov_b32_e32 v17, 0
	s_branch .LBB0_356
